# P1 K-loop: LDS-DMA staging loads issued at the head of each load segment before the fragment ds_reads
# baseline (speedup 1.0000x reference)
.LBB0_186:
	s_add_u32 s0, s30, 0xfffc0080
	s_addc_u32 s1, s31, -1
	s_cmp_eq_u32 s55, 12
	s_cselect_b32 s37, s7, s1
	s_cselect_b32 s36, s9, s0
	s_cselect_b32 s35, s21, s54
	s_cselect_b32 s34, s23, s53
	v_lshl_add_u64 v[184:185], s[30:31], 0, v[176:177]
	s_add_i32 m0, s29, 0xc000
	s_nop 0
	global_load_lds_dwordx4 v[184:185], off
	v_lshl_add_u64 v[184:185], s[30:31], 0, v[178:179]
	s_add_i32 m0, s29, 0xe000
	s_nop 0
	global_load_lds_dwordx4 v[184:185], off
	ds_read_b128 v[26:29], v191
	ds_read_b128 v[30:33], v191 offset:1024
	ds_read_b128 v[18:21], v191 offset:2048
	ds_read_b128 v[22:25], v191 offset:3072
	ds_read_b128 v[10:13], v192
	ds_read_b128 v[14:17], v192 offset:1024
	ds_read_b128 v[2:5], v192 offset:2048
	ds_read_b128 v[6:9], v192 offset:3072
	ds_read_b128 v[196:199], v193
	ds_read_b128 v[200:203], v193 offset:1024
	ds_read_b128 v[204:207], v193 offset:2048
	ds_read_b128 v[208:211], v193 offset:3072
	ds_read_b128 v[212:215], v193 offset:4096
	ds_read_b128 v[216:219], v193 offset:5120
	ds_read_b128 v[220:223], v193 offset:6144
	ds_read_b128 v[224:227], v193 offset:7168
	s_and_b64 vcc, exec, s[14:15]
	s_cbranch_vccnz .Lwa_186l_0
	s_waitcnt vmcnt(8)

.Lwb_186l_0:
	s_setprio 0
	s_barrier
	s_add_i32 s0, s49, s40
	v_lshl_add_u64 v[184:185], s[34:35], 0, v[164:165]
	s_mov_b32 m0, s0
	s_nop 0
	global_load_lds_dwordx4 v[184:185], off
	s_add_i32 m0, s0, 0x2000
	s_add_u32 s56, s34, 0x40000
	v_lshl_add_u64 v[184:185], s[34:35], 0, v[168:169]
	s_addc_u32 s57, s35, 0
	s_add_i32 s0, s50, s40
	global_load_lds_dwordx4 v[184:185], off
	v_lshl_add_u64 v[184:185], s[56:57], 0, v[164:165]
	s_mov_b32 m0, s0
	v_lshl_add_u64 v[186:187], s[36:37], 0, v[166:167]
	global_load_lds_dwordx4 v[184:185], off
	v_lshl_add_u64 v[184:185], s[56:57], 0, v[168:169]
	s_add_i32 m0, s0, 0x2000
	s_nop 0
	global_load_lds_dwordx4 v[184:185], off
	v_lshl_add_u64 v[184:185], s[36:37], 0, v[162:163]
	s_mov_b32 m0, s29
	s_nop 0
	global_load_lds_dwordx4 v[184:185], off
	s_mov_b32 m0, s41
	s_nop 0
	global_load_lds_dwordx4 v[186:187], off
	ds_read_b128 v[196:199], v193 offset:16384
	ds_read_b128 v[200:203], v193 offset:17408
	ds_read_b128 v[204:207], v193 offset:18432
	ds_read_b128 v[208:211], v193 offset:19456
	ds_read_b128 v[212:215], v193 offset:20480
	ds_read_b128 v[216:219], v193 offset:21504
	ds_read_b128 v[220:223], v193 offset:22528
	ds_read_b128 v[224:227], v193 offset:23552
	s_and_b64 vcc, exec, s[14:15]
	s_cbranch_vccnz .Lwa_186l_1
	s_waitcnt vmcnt(8)

.Lmid_186:
	s_add_i32 s0, 0, 0x18000
	v_add_u32_e32 v0, s0, v189
	s_add_i32 s1, 0, 0x1c000
	ds_read_b128 v[2:5], v0
	ds_read_b128 v[6:9], v0 offset:1024
	ds_read_b128 v[10:13], v0 offset:2048
	ds_read_b128 v[14:17], v0 offset:3072
	v_add_u32_e32 v0, s1, v189
	ds_read_b128 v[18:21], v0
	ds_read_b128 v[22:25], v0 offset:1024
	ds_read_b128 v[26:29], v0 offset:2048
	ds_read_b128 v[30:33], v0 offset:3072
	s_add_u32 s36, s36, 0x40000
	s_addc_u32 s37, s37, 0
	s_mov_b32 m0, s42
	v_lshl_add_u64 v[228:229], s[36:37], 0, v[162:163]
	global_load_lds_dwordx4 v[228:229], off
	v_lshl_add_u64 v[228:229], s[36:37], 0, v[166:167]
	s_mov_b32 m0, s43
	s_nop 0
	global_load_lds_dwordx4 v[228:229], off
	ds_read_b128 v[196:199], v193 offset:32768
	ds_read_b128 v[200:203], v193 offset:33792
	ds_read_b128 v[204:207], v193 offset:34816
	ds_read_b128 v[208:211], v193 offset:35840
	ds_read_b128 v[212:215], v193 offset:36864
	ds_read_b128 v[216:219], v193 offset:37888
	ds_read_b128 v[220:223], v193 offset:38912
	ds_read_b128 v[224:227], v193 offset:39936
	s_and_b64 vcc, exec, s[14:15]
	s_cbranch_vccnz .Lwa_186l_2
	s_waitcnt vmcnt(8)

.Lwb_186l_2:
	s_setprio 0
	s_barrier
	s_add_u32 s36, s34, 0x2000
	s_addc_u32 s37, s35, 0
	s_add_i32 s0, s0, s40
	v_lshl_add_u64 v[228:229], s[36:37], 0, v[164:165]
	s_mov_b32 m0, s0
	s_nop 0
	global_load_lds_dwordx4 v[228:229], off
	s_add_i32 m0, s0, 0x2000
	s_add_u32 s34, s34, 0x42000
	v_lshl_add_u64 v[228:229], s[36:37], 0, v[168:169]
	s_addc_u32 s35, s35, 0
	s_add_i32 s0, s1, s40
	global_load_lds_dwordx4 v[228:229], off
	v_lshl_add_u64 v[228:229], s[34:35], 0, v[164:165]
	s_mov_b32 m0, s0
	v_lshl_add_u64 v[184:185], v[184:185], 0, s[12:13]
	global_load_lds_dwordx4 v[228:229], off
	v_lshl_add_u64 v[228:229], s[34:35], 0, v[168:169]
	s_add_i32 m0, s0, 0x2000
	s_nop 0
	global_load_lds_dwordx4 v[228:229], off
	s_mov_b32 m0, s44
	s_nop 0
	global_load_lds_dwordx4 v[184:185], off
	v_lshl_add_u64 v[184:185], v[186:187], 0, s[12:13]
	s_mov_b32 m0, s45
	s_nop 0
	global_load_lds_dwordx4 v[184:185], off
	ds_read_b128 v[196:199], v193 offset:49152
	ds_read_b128 v[200:203], v193 offset:50176
	ds_read_b128 v[204:207], v193 offset:51200
	ds_read_b128 v[208:211], v193 offset:52224
	ds_read_b128 v[212:215], v193 offset:53248
	ds_read_b128 v[216:219], v193 offset:54272
	ds_read_b128 v[220:223], v193 offset:55296
	ds_read_b128 v[224:227], v193 offset:56320
	s_and_b64 vcc, exec, s[14:15]
	s_cbranch_vccnz .Lwa_186l_3
	s_waitcnt vmcnt(8)
